# MLA lean step head: LDS base addresses precomputed in the previous step P.V phase, head SALU behind first MFMA, deferred exp2 in QK^T gaps 1-2
# speedup vs baseline: 1.0066x; 1.0042x over previous
; #define LAS __attribute__((address_space(3)))
; __device__ __forceinline__ float ex2(float x) { return __builtin_amdgcn_exp2f(x); }
; __device__ __forceinline__ f32x16 mfma32(bf16x8 a, bf16x8 b, f32x16 c) { return __builtin_amdgcn_mfma_f32_32x32x16_bf16(a, b, c, 0, 0, 0); }
; #define MLA_WAITBAR() do { if (wid < 4) asm volatile("s_waitcnt vmcnt(6) lgkmcnt(0)\n\ts_barrier" ::: "memory"); else asm volatile("s_waitcnt vmcnt(4) lgkmcnt(0)\n\ts_barrier" ::: "memory"); } while (0)
; #define MLA_ISSUE(s) do { const int tk_ = (s) + 3 < NT - 1 ? (s) + 3 : NT - 1, tv_ = (s) + 2 < 0 ? 0 : ((s) + 2 < NT - 1 ? (s) + 2 : NT - 1); MLA_DMAK(tk_, ((s) + 3) & 3); MLA_DMAV(tv_, ((s) + 2) & 3); } while (0)
; #define PIN(x) asm volatile("" : "+v"(x))
; __device__ __forceinline__ void mla_unit(int b, int h, int qb, const bf16_t* __restrict__ Q, const bf16_t* __restrict__ KV, const bf16_t* __restrict__ PROJ, bf16_t* OCAT, float* SSQO, ldsp shm) {
;     ...
;     float mhat = 0.f, l_reg = 0.f; f32x16 o[2]; o[0] = f32x16{}; o[1] = f32x16{}; f32x16 negm = f32x16{};
;     f32x16 pA0, pA1, pB0, pB1;
;     ...
;     MLA_WAITBAR();
;     MLA_ISSUE(0);
;     { const LAS unsigned char* kb = kp0; pA0 = f32x16{}; pA1 = f32x16{};
; #pragma unroll
;       for (int d0 = 0; d0 < 6; ++d0) { const bf16x8 k0 = *(const LAS bf16x8*)(kb + d0 * 2048), k1 = *(const LAS bf16x8*)(kb + d0 * 2048 + 512); pA0 = mfma32(k0, qr[d0], pA0); pA1 = mfma32(k1, qr[d0], pA1); }
;       mhat = rowmax(pA0, pA1);
; #pragma unroll
;       for (int r = 0; r < 16; ++r) { negm[r] = -mhat; pA0[r] = ex2(pA0[r] - mhat); pA1[r] = ex2(pA1[r] - mhat); } }
;     PIN(negm);
.LBB0_1145:
	s_mov_b64 s[10:11], 0x40000
	v_lshlrev_b32_e32 v6, 10, v184
	v_lshlrev_b32_e32 v7, 4, v183
	v_lshl_add_u64 v[4:5], v[4:5], 0, s[10:11]
	s_add_i32 m0, s26, 0x10000
	v_add3_u32 v188, 0, v6, v7
	global_load_lds_dwordx4 v[4:5], off
	ds_read_b128 v[4:7], v188
	ds_read_b128 v[10:13], v188 offset:512
	s_waitcnt vmcnt(0) lgkmcnt(0)
	v_mfma_f32_32x32x16_bf16 v[20:35], v[4:7], v[136:139], 0
	v_lshlrev_b32_e32 v9, 8, v184
	s_and_b32 s8, s2, 0x3fffffc0
	s_lshl_b32 s8, s8, 2
	s_add_i32 s51, s8, 0
	s_mov_b32 s8, s9
	s_mov_b32 s10, s9
	s_mov_b32 s11, s9
	v_mfma_f32_32x32x16_bf16 v[52:67], v[10:13], v[136:139], 0
	ds_read_b128 v[4:7], v188 offset:2048
	ds_read_b128 v[10:13], v188 offset:2560
	s_mov_b32 s12, s9
	s_mov_b32 s13, s9
	s_mov_b32 s14, s9
	s_mov_b32 s15, s9
	s_mov_b32 s16, s9
	s_mov_b32 s17, s9
	s_waitcnt lgkmcnt(1)
	v_mfma_f32_32x32x16_bf16 v[20:35], v[4:7], v[132:135], v[20:35]
	s_mov_b32 s18, s9
	s_mov_b32 s19, s9
	s_mov_b32 s20, s9
	s_mov_b32 s21, s9
	s_mov_b32 s22, s9
	s_mov_b32 s23, s9
	s_lshl_b32 s3, s3, 2
	s_waitcnt lgkmcnt(0)
	v_mfma_f32_32x32x16_bf16 v[52:67], v[10:13], v[132:135], v[52:67]
	ds_read_b128 v[4:7], v188 offset:4096
	ds_read_b128 v[10:13], v188 offset:4608
	s_ashr_i32 s2, s2, 7
	s_add_i32 s51, s51, 0x14000
	s_add_i32 s52, s2, s3
	s_mov_b32 s27, 2
	s_add_i32 s52, s52, 1
	s_or_b32 s2, s3, 3
	s_waitcnt lgkmcnt(1)
	v_mfma_f32_32x32x16_bf16 v[20:35], v[4:7], v[128:131], v[20:35]
	ds_read_b128 v[4:7], v188 offset:6144
	ds_read_b128 v[36:39], v188 offset:10752
	v_cmp_gt_u32_e64 s[36:37], 32, v182
	v_lshl_add_u32 v185, v183, 2, s51
	v_mov_b32_e32 v189, 0
	s_waitcnt lgkmcnt(2)
	v_mfma_f32_32x32x16_bf16 v[52:67], v[10:13], v[128:131], v[52:67]
	ds_read_b128 v[10:13], v188 offset:6656
	s_waitcnt lgkmcnt(2)
	v_mfma_f32_32x32x16_bf16 v[20:35], v[4:7], v[124:127], v[20:35]
	v_lshlrev_b32_e32 v4, 1, v1
	v_and_b32_e32 v4, 32, v4
	v_add3_u32 v8, 0, v4, v8
	v_lshlrev_b32_e32 v4, 4, v1
	v_and_b32_e32 v14, 0xc0, v4
	ds_read_b128 v[4:7], v188 offset:8192
	v_add3_u32 v186, v8, v9, v14
	s_waitcnt lgkmcnt(1)
	v_mfma_f32_32x32x16_bf16 v[52:67], v[10:13], v[124:127], v[52:67]
	ds_read_b128 v[8:11], v188 offset:8704
	s_waitcnt lgkmcnt(1)
	v_mfma_f32_32x32x16_bf16 v[20:35], v[4:7], v[120:123], v[20:35]
	ds_read_b128 v[4:7], v188 offset:10240
	s_waitcnt lgkmcnt(1)
	v_mfma_f32_32x32x16_bf16 v[52:67], v[8:11], v[120:123], v[52:67]
	s_waitcnt lgkmcnt(0)
	v_mfma_f32_32x32x16_bf16 v[20:35], v[4:7], v[116:119], v[20:35]
	v_mov_b64_e32 v[4:5], s[8:9]
	v_mov_b64_e32 v[18:19], s[22:23]
	v_mov_b64_e32 v[6:7], s[10:11]
	v_mov_b64_e32 v[8:9], s[12:13]
	v_mov_b64_e32 v[10:11], s[14:15]
	v_mov_b64_e32 v[12:13], s[16:17]
	v_mov_b64_e32 v[14:15], s[18:19]
	v_mfma_f32_32x32x16_bf16 v[52:67], v[36:39], v[116:119], v[52:67]
	s_nop 3
	v_max_f32_e32 v40, v21, v21
	v_max_f32_e32 v41, v20, v20
	v_max_f32_e32 v40, v41, v40
	v_mov_b64_e32 v[16:17], s[20:21]
	s_mov_b32 s14, 0x8000
	s_nop 2
	v_max3_f32 v36, v22, v23, v53
	v_max3_f32 v37, v40, v52, v54
	v_max3_f32 v37, v37, v55, v24
	v_max3_f32 v36, v36, v26, v27
	v_max3_f32 v37, v37, v25, v56
	v_max3_f32 v36, v36, v58, v59
	v_max3_f32 v37, v37, v57, v28
	v_max3_f32 v36, v36, v30, v31
	v_max3_f32 v37, v37, v29, v60
	v_max3_f32 v36, v36, v62, v63
	v_max3_f32 v37, v37, v61, v32
	v_max3_f32 v36, v36, v34, v35
	v_max3_f32 v37, v37, v33, v64
	v_max3_f32 v36, v36, v66, v67
	v_max3_f32 v36, v37, v65, v36
	v_mov_b32_e32 v37, v36
	s_nop 1
	v_permlane32_swap_b32_e32 v36, v37
	v_max_f32_e32 v37, v37, v37
	v_max_f32_e32 v36, v36, v36
	v_max_f32_e32 v187, v36, v37
	v_sub_f32_e32 v20, v20, v187
	v_exp_f32_e32 v68, v20
	v_sub_f32_e32 v20, v21, v187
	v_exp_f32_e32 v69, v20
	v_sub_f32_e32 v20, v22, v187
	v_exp_f32_e32 v70, v20
	v_sub_f32_e32 v20, v23, v187
	v_exp_f32_e32 v71, v20
	v_sub_f32_e32 v20, v24, v187
	v_exp_f32_e32 v72, v20
	v_sub_f32_e32 v20, v25, v187
	v_exp_f32_e32 v73, v20
	v_sub_f32_e32 v20, v26, v187
	v_exp_f32_e32 v74, v20
	v_sub_f32_e32 v20, v27, v187
	v_exp_f32_e32 v75, v20
	v_sub_f32_e32 v20, v28, v187
	v_exp_f32_e32 v76, v20
	v_sub_f32_e32 v20, v29, v187
	v_exp_f32_e32 v77, v20
	v_sub_f32_e32 v20, v30, v187
	v_exp_f32_e32 v78, v20
	v_sub_f32_e32 v20, v31, v187
	v_exp_f32_e32 v79, v20
	v_sub_f32_e32 v20, v32, v187
	v_exp_f32_e32 v80, v20
	v_sub_f32_e32 v20, v33, v187
	v_exp_f32_e32 v81, v20
	v_sub_f32_e32 v20, v34, v187
	v_sub_f32_e32 v52, v52, v187
	v_sub_f32_e32 v53, v53, v187
	v_sub_f32_e32 v54, v54, v187
	v_sub_f32_e32 v55, v55, v187
	v_sub_f32_e32 v56, v56, v187
	v_sub_f32_e32 v57, v57, v187
	v_sub_f32_e32 v58, v58, v187
	v_sub_f32_e32 v59, v59, v187
	v_sub_f32_e32 v60, v60, v187
	v_sub_f32_e32 v61, v61, v187
	v_sub_f32_e32 v62, v62, v187
	v_sub_f32_e32 v63, v63, v187
	v_sub_f32_e32 v64, v64, v187
	v_sub_f32_e32 v65, v65, v187
	v_sub_f32_e32 v66, v66, v187
	v_sub_f32_e32 v67, v67, v187
	v_exp_f32_e32 v82, v20
	v_sub_f32_e32 v20, v35, v187
	v_exp_f32_e32 v52, v52
	v_exp_f32_e32 v53, v53
	v_exp_f32_e32 v54, v54
	v_exp_f32_e32 v55, v55
	v_exp_f32_e32 v56, v56
	v_exp_f32_e32 v57, v57
	v_exp_f32_e32 v58, v58
	v_exp_f32_e32 v59, v59
	v_exp_f32_e32 v83, v20
	v_xor_b32_e32 v36, 0x80000000, v187
	v_mov_b64_e32 v[34:35], v[18:19]
	v_mov_b32_e32 v37, v36
	v_mov_b32_e32 v38, v36
	v_mov_b32_e32 v39, v36
	v_mov_b32_e32 v40, v36
	v_mov_b32_e32 v41, v36
	v_mov_b32_e32 v42, v36
	v_mov_b32_e32 v43, v36
	v_mov_b32_e32 v44, v36
	v_mov_b32_e32 v45, v36
	v_mov_b32_e32 v46, v36
	v_mov_b32_e32 v47, v36
	v_mov_b32_e32 v48, v36
	v_mov_b32_e32 v49, v36
	v_mov_b32_e32 v50, v36
	v_mov_b32_e32 v51, v36
	v_mov_b64_e32 v[32:33], v[16:17]
	v_mov_b64_e32 v[30:31], v[14:15]
	v_mov_b64_e32 v[28:29], v[12:13]
	v_mov_b64_e32 v[26:27], v[10:11]
	v_mov_b64_e32 v[24:25], v[8:9]
	v_mov_b64_e32 v[22:23], v[6:7]
	v_mov_b64_e32 v[20:21], v[4:5]
	s_add_i32 s12, s27, -1
	s_and_b32 s12, s12, 3
	s_mulk_i32 s12, 0x3000
	v_add_u32_e32 v156, s12, v188
	s_and_b32 s12, s14, 0x6000
	v_add_u32_e32 v157, s12, v186
	s_mov_b64 s[10:11], -1
	s_and_b64 vcc, exec, s[40:41]
	s_cbranch_vccz .LBB0_1147

.LBB0_1149:
	ds_read_b128 v[84:87], v156
	ds_read_b128 v[190:193], v156 offset:512
	ds_read_b128 v[194:197], v156 offset:2048
	ds_read_b128 v[198:201], v156 offset:2560
	s_setprio 1
	s_waitcnt lgkmcnt(0)
	v_mfma_f32_32x32x16_bf16 v[100:115], v[84:87], v[136:139], v[36:51]
	s_add_i32 s19, s27, -1
	s_and_b32 s18, s19, 3
	s_mul_i32 s20, s18, 0x3000
	s_and_b32 s17, s14, 0x6000
	v_add_f32_e32 v88, v68, v69
	ds_read_b128 v[202:205], v156 offset:4096
	ds_read_b64_tr_b16 v[172:173], v157 offset:49152
	ds_read_b64_tr_b16 v[174:175], v157 offset:49664
	v_add_f32_e32 v84, v70, v88
	v_add_f32_e32 v84, v71, v84
	v_add_f32_e32 v84, v72, v84
	v_add_f32_e32 v144, v73, v84
	v_cvt_pk_bf16_f32 v140, v68, v69
	v_cvt_pk_bf16_f32 v141, v70, v71
	v_exp_f32_e32 v60, v60
	v_exp_f32_e32 v61, v61
	v_exp_f32_e32 v62, v62
	v_exp_f32_e32 v63, v63
	v_mfma_f32_32x32x16_bf16 v[84:99], v[190:193], v[136:139], v[36:51]
	ds_read_b128 v[190:193], v156 offset:4608
	ds_read_b64_tr_b16 v[68:69], v157 offset:53248
	ds_read_b64_tr_b16 v[70:71], v157 offset:53760
	v_add_f32_e32 v142, v74, v144
	v_add_f32_e32 v142, v75, v142
	v_add_f32_e32 v142, v76, v142
	v_add_f32_e32 v144, v77, v142
	v_cvt_pk_bf16_f32 v142, v72, v73
	v_cvt_pk_bf16_f32 v143, v74, v75
	v_exp_f32_e32 v64, v64
	v_exp_f32_e32 v65, v65
	v_exp_f32_e32 v66, v66
	v_exp_f32_e32 v67, v67
	v_mfma_f32_32x32x16_bf16 v[100:115], v[194:197], v[132:135], v[100:115]
	ds_read_b128 v[194:197], v156 offset:6144
	ds_read_b64_tr_b16 v[72:73], v157 offset:50176
	ds_read_b64_tr_b16 v[74:75], v157 offset:50688
	v_add_f32_e32 v144, v78, v144
	v_add_f32_e32 v144, v79, v144
	v_add_f32_e32 v144, v80, v144
	v_add_f32_e32 v148, v81, v144
	v_cvt_pk_bf16_f32 v144, v76, v77
	v_cvt_pk_bf16_f32 v145, v78, v79
	v_mfma_f32_32x32x16_bf16 v[84:99], v[198:201], v[132:135], v[84:99]
	ds_read_b128 v[198:201], v156 offset:6656
	ds_read_b64_tr_b16 v[76:77], v157 offset:54272
	ds_read_b64_tr_b16 v[78:79], v157 offset:54784
	v_add_f32_e32 v146, v82, v148
	v_add_f32_e32 v146, v83, v146
	v_add_f32_e32 v146, v52, v146
	v_add_f32_e32 v148, v53, v146
	v_cvt_pk_bf16_f32 v146, v80, v81
	v_cvt_pk_bf16_f32 v147, v82, v83
	s_waitcnt lgkmcnt(0)
	v_mfma_f32_32x32x16_bf16 v[100:115], v[202:205], v[128:131], v[100:115]
	ds_read_b128 v[202:205], v156 offset:8192
	ds_read_b64_tr_b16 v[80:81], v157 offset:51200
	ds_read_b64_tr_b16 v[82:83], v157 offset:51712
	v_add_f32_e32 v148, v54, v148
	v_add_f32_e32 v148, v55, v148
	v_add_f32_e32 v148, v56, v148
	v_add_f32_e32 v152, v57, v148
	v_cvt_pk_bf16_f32 v148, v52, v53
	v_cvt_pk_bf16_f32 v149, v54, v55
	v_mfma_f32_32x32x16_bf16 v[84:99], v[190:193], v[128:131], v[84:99]
	ds_read_b128 v[190:193], v156 offset:8704
	ds_read_b64_tr_b16 v[52:53], v157 offset:55296
	ds_read_b64_tr_b16 v[54:55], v157 offset:55808
	v_add_f32_e32 v150, v58, v152
	v_add_f32_e32 v150, v59, v150
	v_add_f32_e32 v150, v60, v150
	v_add_f32_e32 v152, v61, v150
	v_cvt_pk_bf16_f32 v150, v56, v57
	v_cvt_pk_bf16_f32 v151, v58, v59
	v_mfma_f32_32x32x16_bf16 v[100:115], v[194:197], v[124:127], v[100:115]
	ds_read_b128 v[194:197], v156 offset:10240
	ds_read_b64_tr_b16 v[56:57], v157 offset:52224
	ds_read_b64_tr_b16 v[58:59], v157 offset:52736
	v_add_f32_e32 v152, v62, v152
	v_add_f32_e32 v152, v63, v152
	v_add_f32_e32 v152, v64, v152
	v_add_f32_e32 v160, v65, v152
	v_cvt_pk_bf16_f32 v152, v60, v61
	v_cvt_pk_bf16_f32 v153, v62, v63
	v_mfma_f32_32x32x16_bf16 v[84:99], v[198:201], v[124:127], v[84:99]
	ds_read_b128 v[198:201], v156 offset:10752
	ds_read_b64_tr_b16 v[60:61], v157 offset:56320
	ds_read_b64_tr_b16 v[62:63], v157 offset:56832
	v_add_f32_e32 v154, v66, v160
	v_add_f32_e32 v156, v67, v154
	v_cvt_pk_bf16_f32 v154, v64, v65
	v_cvt_pk_bf16_f32 v155, v66, v67
	s_waitcnt lgkmcnt(0)
	v_mfma_f32_32x32x16_bf16 v[100:115], v[202:205], v[120:123], v[100:115]
	s_add_i32 s16, s27, 2
	s_min_i32 s8, s16, s2
	s_lshl_b64 s[10:11], s[8:9], 17
	v_lshl_add_u64 v[202:203], v[176:177], 0, s[10:11]
	s_and_b32 s10, s16, 3
	s_mulk_i32 s10, 0x3000
	s_add_i32 s10, s26, s10
	s_mov_b32 m0, s10
	s_nop 0
	global_load_lds_dwordx4 v[202:203], off
	v_mfma_f32_32x32x16_bf16 v[84:99], v[190:193], v[120:123], v[84:99]
	s_and_b64 vcc, exec, s[38:39]
	s_cbranch_vccnz .Lmla_rope1
	s_lshl_b64 s[12:13], s[8:9], 18
	v_lshl_add_u64 v[202:203], v[180:181], 0, s[12:13]
	s_add_i32 m0, s10, 0x2000
	s_nop 0
	global_load_lds_dwordx4 v[202:203], off

.LBB0_1153:
	v_mfma_f32_32x32x16_bf16 v[4:19], v[140:143], v[172:175], v[4:19]
	v_exp_f32_e32 v100, v100
	v_exp_f32_e32 v101, v101
	v_exp_f32_e32 v102, v102
	v_exp_f32_e32 v103, v103
	v_mfma_f32_32x32x16_bf16 v[20:35], v[140:143], v[68:71], v[20:35]
	v_exp_f32_e32 v104, v104
	v_exp_f32_e32 v105, v105
	v_exp_f32_e32 v106, v106
	v_exp_f32_e32 v107, v107
	s_and_b32 s12, s27, 3
	s_mulk_i32 s12, 0x3000
	v_add_u32_e32 v140, s12, v188
	v_lshl_add_u32 v141, s18, 13, v186
	v_mfma_f32_32x32x16_bf16 v[4:19], v[144:147], v[72:75], v[4:19]
	v_exp_f32_e32 v108, v108
	v_exp_f32_e32 v109, v109
	v_exp_f32_e32 v110, v110
	v_exp_f32_e32 v111, v111
	v_mfma_f32_32x32x16_bf16 v[20:35], v[144:147], v[76:79], v[20:35]
	v_exp_f32_e32 v112, v112
	v_exp_f32_e32 v113, v113
	v_exp_f32_e32 v114, v114
	v_exp_f32_e32 v115, v115
	v_mfma_f32_32x32x16_bf16 v[4:19], v[148:151], v[80:83], v[4:19]
	v_exp_f32_e32 v84, v84
	v_exp_f32_e32 v85, v85
	v_exp_f32_e32 v86, v86
	v_exp_f32_e32 v87, v87
	v_mfma_f32_32x32x16_bf16 v[20:35], v[148:151], v[52:55], v[20:35]
	v_exp_f32_e32 v88, v88
	v_exp_f32_e32 v89, v89
	v_exp_f32_e32 v90, v90
	v_exp_f32_e32 v91, v91
	v_mfma_f32_32x32x16_bf16 v[4:19], v[152:155], v[56:59], v[4:19]
	v_mfma_f32_32x32x16_bf16 v[20:35], v[152:155], v[60:63], v[20:35]
	s_andn2_b64 vcc, exec, s[10:11]
	s_cbranch_vccnz .LBB0_1155
	s_waitcnt lgkmcnt(0)
	v_add_u32_e32 v64, s51, v2
	ds_read_b128 v[52:55], v64 offset:96
	ds_read_b128 v[56:59], v64 offset:64
	ds_read_b128 v[60:63], v64 offset:32
	ds_read_b128 v[64:67], v64
	s_waitcnt lgkmcnt(0)
	v_pk_mul_f32 v[16:17], v[16:17], v[52:53]
	v_pk_mul_f32 v[12:13], v[12:13], v[56:57]
	v_pk_mul_f32 v[8:9], v[8:9], v[60:61]
	v_pk_mul_f32 v[18:19], v[18:19], v[54:55]
	v_pk_mul_f32 v[14:15], v[14:15], v[58:59]
	v_pk_mul_f32 v[10:11], v[10:11], v[62:63]
	v_pk_mul_f32 v[6:7], v[6:7], v[66:67]
	v_pk_mul_f32 v[4:5], v[4:5], v[64:65]
	v_pk_mul_f32 v[32:33], v[32:33], v[52:53]
	v_pk_mul_f32 v[28:29], v[28:29], v[56:57]
	v_pk_mul_f32 v[24:25], v[24:25], v[60:61]
	v_pk_mul_f32 v[34:35], v[34:35], v[54:55]
	v_pk_mul_f32 v[30:31], v[30:31], v[58:59]
	v_pk_mul_f32 v[26:27], v[26:27], v[62:63]
	v_pk_mul_f32 v[22:23], v[22:23], v[66:67]
	v_pk_mul_f32 v[20:21], v[20:21], v[64:65]

.LBB0_1159:
	ds_read_b128 v[52:55], v140
	ds_read_b128 v[190:193], v140 offset:512
	ds_read_b128 v[194:197], v140 offset:2048
	ds_read_b128 v[198:201], v140 offset:2560
	s_setprio 1
	s_waitcnt lgkmcnt(0)
	v_mfma_f32_32x32x16_bf16 v[68:83], v[52:55], v[136:139], v[36:51]
	v_add_f32_e32 v56, v100, v101
	ds_read_b128 v[202:205], v140 offset:4096
	ds_read_b64_tr_b16 v[172:173], v141 offset:49152
	ds_read_b64_tr_b16 v[174:175], v141 offset:49664
	v_add_f32_e32 v52, v102, v56
	v_add_f32_e32 v52, v103, v52
	v_add_f32_e32 v52, v104, v52
	v_add_f32_e32 v144, v105, v52
	v_cvt_pk_bf16_f32 v156, v100, v101
	v_cvt_pk_bf16_f32 v157, v102, v103
	v_exp_f32_e32 v92, v92
	v_exp_f32_e32 v93, v93
	v_exp_f32_e32 v94, v94
	v_exp_f32_e32 v95, v95
	v_mfma_f32_32x32x16_bf16 v[52:67], v[190:193], v[136:139], v[36:51]
	ds_read_b128 v[190:193], v140 offset:4608
	ds_read_b64_tr_b16 v[100:101], v141 offset:53248
	ds_read_b64_tr_b16 v[102:103], v141 offset:53760
	v_add_f32_e32 v144, v106, v144
	v_add_f32_e32 v144, v107, v144
	v_add_f32_e32 v144, v108, v144
	v_add_f32_e32 v144, v109, v144
	v_cvt_pk_bf16_f32 v158, v104, v105
	v_cvt_pk_bf16_f32 v159, v106, v107
	v_exp_f32_e32 v96, v96
	v_exp_f32_e32 v97, v97
	v_exp_f32_e32 v98, v98
	v_exp_f32_e32 v99, v99
	v_mfma_f32_32x32x16_bf16 v[68:83], v[194:197], v[132:135], v[68:83]
	ds_read_b128 v[194:197], v140 offset:6144
	ds_read_b64_tr_b16 v[104:105], v141 offset:50176
	ds_read_b64_tr_b16 v[106:107], v141 offset:50688
	v_add_f32_e32 v144, v110, v144
	v_add_f32_e32 v144, v111, v144
	v_add_f32_e32 v144, v112, v144
	v_add_f32_e32 v144, v113, v144
	v_cvt_pk_bf16_f32 v160, v108, v109
	v_cvt_pk_bf16_f32 v161, v110, v111
	v_mfma_f32_32x32x16_bf16 v[52:67], v[198:201], v[132:135], v[52:67]
	ds_read_b128 v[198:201], v140 offset:6656
	ds_read_b64_tr_b16 v[108:109], v141 offset:54272
	ds_read_b64_tr_b16 v[110:111], v141 offset:54784
	v_add_f32_e32 v144, v114, v144
	v_add_f32_e32 v144, v115, v144
	v_add_f32_e32 v144, v84, v144
	v_add_f32_e32 v144, v85, v144
	v_cvt_pk_bf16_f32 v162, v112, v113
	v_cvt_pk_bf16_f32 v163, v114, v115
	s_waitcnt lgkmcnt(0)
	v_mfma_f32_32x32x16_bf16 v[68:83], v[202:205], v[128:131], v[68:83]
	ds_read_b128 v[202:205], v140 offset:8192
	ds_read_b64_tr_b16 v[112:113], v141 offset:51200
	ds_read_b64_tr_b16 v[114:115], v141 offset:51712
	v_add_f32_e32 v144, v86, v144
	v_add_f32_e32 v144, v87, v144
	v_add_f32_e32 v144, v88, v144
	v_add_f32_e32 v144, v89, v144
	v_cvt_pk_bf16_f32 v164, v84, v85
	v_cvt_pk_bf16_f32 v165, v86, v87
	v_mfma_f32_32x32x16_bf16 v[52:67], v[190:193], v[128:131], v[52:67]
	ds_read_b128 v[190:193], v140 offset:8704
	ds_read_b64_tr_b16 v[84:85], v141 offset:55296
	ds_read_b64_tr_b16 v[86:87], v141 offset:55808
	v_add_f32_e32 v144, v90, v144
	v_add_f32_e32 v144, v91, v144
	v_add_f32_e32 v144, v92, v144
	v_add_f32_e32 v144, v93, v144
	v_cvt_pk_bf16_f32 v166, v88, v89
	v_cvt_pk_bf16_f32 v167, v90, v91
	v_mfma_f32_32x32x16_bf16 v[68:83], v[194:197], v[124:127], v[68:83]
	ds_read_b128 v[194:197], v140 offset:10240
	ds_read_b64_tr_b16 v[88:89], v141 offset:52224
	ds_read_b64_tr_b16 v[90:91], v141 offset:52736
	v_add_f32_e32 v144, v94, v144
	v_add_f32_e32 v144, v95, v144
	v_add_f32_e32 v144, v96, v144
	v_add_f32_e32 v144, v97, v144
	v_cvt_pk_bf16_f32 v168, v92, v93
	v_cvt_pk_bf16_f32 v169, v94, v95
	v_mfma_f32_32x32x16_bf16 v[52:67], v[198:201], v[124:127], v[52:67]
	ds_read_b128 v[198:201], v140 offset:10752
	ds_read_b64_tr_b16 v[92:93], v141 offset:56320
	ds_read_b64_tr_b16 v[94:95], v141 offset:56832
	v_add_f32_e32 v140, v98, v144
	v_add_f32_e32 v140, v99, v140
	v_cvt_pk_bf16_f32 v170, v96, v97
	v_cvt_pk_bf16_f32 v171, v98, v99
	s_waitcnt lgkmcnt(0)
	v_mfma_f32_32x32x16_bf16 v[68:83], v[202:205], v[120:123], v[68:83]
	s_add_i32 s8, s27, 3
	s_min_i32 s8, s8, s2
	s_lshl_b64 s[10:11], s[8:9], 17
	v_lshl_add_u64 v[202:203], v[176:177], 0, s[10:11]
	s_add_i32 s10, s26, s20
	s_mov_b32 m0, s10
	s_nop 0
	global_load_lds_dwordx4 v[202:203], off
	v_mfma_f32_32x32x16_bf16 v[52:67], v[190:193], v[120:123], v[52:67]
	s_and_b64 vcc, exec, s[38:39]
	s_cbranch_vccnz .Lmla_rope2
	s_lshl_b64 s[12:13], s[8:9], 18
	v_lshl_add_u64 v[202:203], v[180:181], 0, s[12:13]
	s_add_i32 m0, s10, 0x2000
	s_nop 0
	global_load_lds_dwordx4 v[202:203], off

.LBB0_1163:
	v_mfma_f32_32x32x16_bf16 v[4:19], v[156:159], v[172:175], v[4:19]
	v_exp_f32_e32 v68, v68
	v_exp_f32_e32 v69, v69
	v_exp_f32_e32 v70, v70
	v_exp_f32_e32 v71, v71
	v_mfma_f32_32x32x16_bf16 v[20:35], v[156:159], v[100:103], v[20:35]
	v_exp_f32_e32 v72, v72
	v_exp_f32_e32 v73, v73
	v_exp_f32_e32 v74, v74
	v_exp_f32_e32 v75, v75
	s_add_i32 s12, s16, -1
	s_and_b32 s12, s12, 3
	s_mulk_i32 s12, 0x3000
	v_add_u32_e32 v156, s12, v188
	s_add_i32 s12, s14, 0x4000
	s_and_b32 s12, s12, 0x6000
	v_add_u32_e32 v157, s12, v186
	v_mfma_f32_32x32x16_bf16 v[4:19], v[160:163], v[104:107], v[4:19]
	v_exp_f32_e32 v76, v76
	v_exp_f32_e32 v77, v77
	v_exp_f32_e32 v78, v78
	v_exp_f32_e32 v79, v79
	v_mfma_f32_32x32x16_bf16 v[20:35], v[160:163], v[108:111], v[20:35]
	v_exp_f32_e32 v80, v80
	v_exp_f32_e32 v81, v81
	v_exp_f32_e32 v82, v82
	v_exp_f32_e32 v83, v83
	v_mfma_f32_32x32x16_bf16 v[4:19], v[164:167], v[112:115], v[4:19]
	v_exp_f32_e32 v52, v52
	v_exp_f32_e32 v53, v53
	v_exp_f32_e32 v54, v54
	v_exp_f32_e32 v55, v55
	v_mfma_f32_32x32x16_bf16 v[20:35], v[164:167], v[84:87], v[20:35]
	v_exp_f32_e32 v56, v56
	v_exp_f32_e32 v57, v57
	v_exp_f32_e32 v58, v58
	v_exp_f32_e32 v59, v59
	v_mfma_f32_32x32x16_bf16 v[4:19], v[168:171], v[88:91], v[4:19]
	v_mfma_f32_32x32x16_bf16 v[20:35], v[168:171], v[92:95], v[20:35]
	s_andn2_b64 vcc, exec, s[10:11]
	s_cbranch_vccnz .LBB0_1165
	s_waitcnt lgkmcnt(0)
	v_add_u32_e32 v96, s51, v2
	ds_read_b128 v[84:87], v96 offset:96
	ds_read_b128 v[88:91], v96 offset:64
	ds_read_b128 v[92:95], v96 offset:32
	ds_read_b128 v[96:99], v96
	s_waitcnt lgkmcnt(0)
	v_pk_mul_f32 v[16:17], v[16:17], v[84:85]
	v_pk_mul_f32 v[12:13], v[12:13], v[88:89]
	v_pk_mul_f32 v[8:9], v[8:9], v[92:93]
	v_pk_mul_f32 v[18:19], v[18:19], v[86:87]
	v_pk_mul_f32 v[14:15], v[14:15], v[90:91]
	v_pk_mul_f32 v[10:11], v[10:11], v[94:95]
	v_pk_mul_f32 v[6:7], v[6:7], v[98:99]
	v_pk_mul_f32 v[4:5], v[4:5], v[96:97]
	v_pk_mul_f32 v[32:33], v[32:33], v[84:85]
	v_pk_mul_f32 v[28:29], v[28:29], v[88:89]
	v_pk_mul_f32 v[24:25], v[24:25], v[92:93]
	v_pk_mul_f32 v[34:35], v[34:35], v[86:87]
	v_pk_mul_f32 v[30:31], v[30:31], v[90:91]
	v_pk_mul_f32 v[26:27], v[26:27], v[94:95]
	v_pk_mul_f32 v[22:23], v[22:23], v[98:99]
	v_pk_mul_f32 v[20:21], v[20:21], v[96:97]

; __device__ __forceinline__ void mla_unit(int b, int h, int qb, const bf16_t* __restrict__ Q, const bf16_t* __restrict__ KV, const bf16_t* __restrict__ PROJ, bf16_t* OCAT, float* SSQO, ldsp shm) {
;     ...
;     STEP(pB0, pB1, pA0, pA1, t);
.LBB0_1179:
	ds_read_b128 v[100:103], v156
	ds_read_b128 v[104:107], v156 offset:512
	ds_read_b128 v[108:111], v156 offset:2048
	ds_read_b128 v[112:115], v156 offset:2560
	s_add_i32 s3, s17, 0
	s_lshl_b32 s8, s2, 17
	s_add_i32 s3, s3, s34
	v_lshl_add_u64 v[84:85], v[176:177], 0, s[8:9]
	s_mov_b32 m0, s3
	s_and_b64 vcc, exec, s[38:39]
	global_load_lds_dwordx4 v[84:85], off
	s_cbranch_vccnz .LBB0_1181
	s_lshl_b32 s10, s2, 18
	s_mov_b32 s11, s9
	v_lshl_add_u64 v[84:85], v[180:181], 0, s[10:11]
	s_add_i32 m0, s3, 0x2000
	s_nop 0
	global_load_lds_dwordx4 v[84:85], off
.LBB0_1181:
	s_xor_b32 s2, s15, 0x4000
	s_add_i32 s2, s2, 0
	v_lshl_add_u64 v[84:85], v[178:179], 0, s[8:9]
	s_add_i32 s2, s2, s34
	v_lshl_add_u64 v[84:85], v[84:85], 0, s[24:25]
	s_add_i32 m0, s2, 0xc000
	s_and_b32 s2, s12, 3
	global_load_lds_dwordx4 v[84:85], off
	s_mulk_i32 s2, 0x3000
	s_and_b32 s2, s14, 0x6000
	s_setprio 1
	s_waitcnt lgkmcnt(0)
	v_mfma_f32_32x32x16_bf16 v[84:99], v[100:103], v[136:139], v[36:51]
	v_add_f32_e32 v144, v68, v69
	ds_read_b128 v[140:143], v156 offset:4096
	ds_read_b64_tr_b16 v[100:101], v157 offset:49152
	ds_read_b64_tr_b16 v[102:103], v157 offset:49664
	v_add_f32_e32 v144, v70, v144
	v_add_f32_e32 v144, v71, v144
	v_add_f32_e32 v144, v72, v144
	v_add_f32_e32 v144, v73, v144
	v_cvt_pk_bf16_f32 v68, v68, v69
	v_cvt_pk_bf16_f32 v69, v70, v71
	v_exp_f32_e32 v60, v60
	v_exp_f32_e32 v61, v61
	v_exp_f32_e32 v62, v62
	v_exp_f32_e32 v63, v63
	v_mfma_f32_32x32x16_bf16 v[36:51], v[104:107], v[136:139], v[36:51]
	ds_read_b128 v[136:139], v156 offset:4608
	ds_read_b64_tr_b16 v[104:105], v157 offset:53248
	ds_read_b64_tr_b16 v[106:107], v157 offset:53760
	v_add_f32_e32 v70, v74, v144
	v_add_f32_e32 v70, v75, v70
	v_add_f32_e32 v70, v76, v70
	v_add_f32_e32 v148, v77, v70
	v_cvt_pk_bf16_f32 v70, v72, v73
	v_cvt_pk_bf16_f32 v71, v74, v75
	v_exp_f32_e32 v64, v64
	v_exp_f32_e32 v65, v65
	v_exp_f32_e32 v66, v66
	v_exp_f32_e32 v67, v67
	v_mfma_f32_32x32x16_bf16 v[84:99], v[108:111], v[132:135], v[84:99]
	ds_read_b128 v[144:147], v156 offset:6144
	ds_read_b64_tr_b16 v[108:109], v157 offset:50176
	ds_read_b64_tr_b16 v[110:111], v157 offset:50688
	v_add_f32_e32 v72, v78, v148
	v_add_f32_e32 v72, v79, v72
	v_add_f32_e32 v72, v80, v72
	v_add_f32_e32 v152, v81, v72
	v_cvt_pk_bf16_f32 v72, v76, v77
	v_cvt_pk_bf16_f32 v73, v78, v79
	v_mfma_f32_32x32x16_bf16 v[36:51], v[112:115], v[132:135], v[36:51]
	ds_read_b128 v[148:151], v156 offset:6656
	ds_read_b64_tr_b16 v[76:77], v157 offset:54272
	ds_read_b64_tr_b16 v[78:79], v157 offset:54784
	v_add_f32_e32 v74, v82, v152
	v_add_f32_e32 v74, v83, v74
	v_add_f32_e32 v74, v52, v74
	v_add_f32_e32 v132, v53, v74
	v_cvt_pk_bf16_f32 v74, v80, v81
	v_cvt_pk_bf16_f32 v75, v82, v83
	s_waitcnt lgkmcnt(0)
	v_mfma_f32_32x32x16_bf16 v[84:99], v[140:143], v[128:131], v[84:99]
	ds_read_b128 v[140:143], v156 offset:8192
	ds_read_b64_tr_b16 v[112:113], v157 offset:51200
	ds_read_b64_tr_b16 v[114:115], v157 offset:51712
	v_add_f32_e32 v80, v54, v132
	v_add_f32_e32 v80, v55, v80
	v_add_f32_e32 v80, v56, v80
	v_add_f32_e32 v132, v57, v80
	v_cvt_pk_bf16_f32 v80, v52, v53
	v_cvt_pk_bf16_f32 v81, v54, v55
	v_mfma_f32_32x32x16_bf16 v[36:51], v[136:139], v[128:131], v[36:51]
	ds_read_b128 v[152:155], v156 offset:8704
	ds_read_b64_tr_b16 v[128:129], v157 offset:55296
	ds_read_b64_tr_b16 v[130:131], v157 offset:55808
	v_add_f32_e32 v52, v58, v132
	v_add_f32_e32 v52, v59, v52
	v_add_f32_e32 v52, v60, v52
	v_add_f32_e32 v52, v61, v52
	v_cvt_pk_bf16_f32 v82, v56, v57
	v_cvt_pk_bf16_f32 v83, v58, v59
	v_mfma_f32_32x32x16_bf16 v[84:99], v[144:147], v[124:127], v[84:99]
	ds_read_b128 v[54:57], v156 offset:10240
	ds_read_b64_tr_b16 v[136:137], v157 offset:52224
	ds_read_b64_tr_b16 v[138:139], v157 offset:52736
	v_add_f32_e32 v52, v62, v52
	v_add_f32_e32 v52, v63, v52
	v_add_f32_e32 v52, v64, v52
	v_add_f32_e32 v52, v65, v52
	v_cvt_pk_bf16_f32 v132, v60, v61
	v_cvt_pk_bf16_f32 v133, v62, v63
	v_mfma_f32_32x32x16_bf16 v[36:51], v[148:151], v[124:127], v[36:51]
	ds_read_b128 v[58:61], v156 offset:10752
	ds_read_b64_tr_b16 v[124:125], v157 offset:56320
	ds_read_b64_tr_b16 v[126:127], v157 offset:56832
	v_add_f32_e32 v52, v66, v52
	v_add_f32_e32 v52, v67, v52
	v_cvt_pk_bf16_f32 v134, v64, v65
	v_cvt_pk_bf16_f32 v135, v66, v67
	s_waitcnt lgkmcnt(0)
	v_mfma_f32_32x32x16_bf16 v[84:99], v[140:143], v[120:123], v[84:99]
	v_mfma_f32_32x32x16_bf16 v[36:51], v[152:155], v[120:123], v[36:51]
	v_mfma_f32_32x32x16_bf16 v[84:99], v[54:57], v[116:119], v[84:99]
	v_mfma_f32_32x32x16_bf16 v[36:51], v[58:61], v[116:119], v[36:51]
	s_setprio 0
	s_cmp_lt_i32 s12, s52
	s_cbranch_scc0 .LBB0_1195
